# MoE GEMM1 fp6 operands read into 8-reg slots (no v_mov), weight-tile LDS-DMA issue moved from load segments into MFMA segments with re-derived vmcnt, MLA row-max via v_max3
# speedup vs baseline: 1.0055x; 1.0055x over previous
.LBB0_1995:
	s_cmp_lt_i32 s88, 1
	v_add_u32_e32 v51, 0x10000, v226
	v_add_u32_e32 v52, 0x14000, v226
	v_add_u32_e32 v53, 0x18000, v226
	v_add_u32_e32 v229, 0x1c000, v226
	s_cbranch_scc1 .LBB0_1997
	ds_read_b128 v[2:5], v51
	ds_read_b128 v[6:9], v51 offset:1024
	ds_read_b128 v[10:13], v51 offset:2048
	ds_read_b128 v[14:17], v51 offset:3072
	ds_read_b128 v[18:21], v52
	ds_read_b128 v[22:25], v52 offset:1024
	ds_read_b128 v[26:29], v52 offset:2048
	ds_read_b128 v[30:33], v52 offset:3072
	s_add_u32 s26, s6, 0x100
	s_addc_u32 s27, s7, 0
	ds_read_b128 v[34:37], v227
	ds_read_b128 v[38:41], v227 offset:1024
	ds_read_b128 v[42:45], v227 offset:2048
	ds_read_b128 v[46:49], v227 offset:3072
	ds_read_b128 v[182:185], v227 offset:4096
	ds_read_b128 v[186:189], v227 offset:5120
	ds_read_b128 v[190:193], v227 offset:6144
	ds_read_b128 v[194:197], v227 offset:7168
	s_mov_b32 m0, s62
	s_nop 0
	global_load_lds_dwordx4 v220, s[8:9]
	s_nop 0
	s_mov_b32 m0, s63
	s_nop 0
	global_load_lds_dwordx4 v222, s[8:9]
	s_waitcnt vmcnt(16)
	s_waitcnt lgkmcnt(0)
	s_barrier
	s_setprio 1
	v_mfma_scale_f32_16x16x128_f8f6f4 v[178:181], v[2:7], v[34:39], v[178:181], v8, v40 op_sel_hi:[0,0,0] cbsz:2 blgp:2
	v_mfma_scale_f32_16x16x128_f8f6f4 v[174:177], v[10:15], v[34:39], v[174:177], v16, v40 op_sel_hi:[0,0,0] cbsz:2 blgp:2
	v_mfma_scale_f32_16x16x128_f8f6f4 v[170:173], v[2:7], v[42:47], v[170:173], v8, v48 op_sel_hi:[0,0,0] cbsz:2 blgp:2
	v_mfma_scale_f32_16x16x128_f8f6f4 v[166:169], v[10:15], v[42:47], v[166:169], v16, v48 op_sel_hi:[0,0,0] cbsz:2 blgp:2
	v_mfma_scale_f32_16x16x128_f8f6f4 v[162:165], v[2:7], v[182:187], v[162:165], v8, v188 op_sel_hi:[0,0,0] cbsz:2 blgp:2
	v_mfma_scale_f32_16x16x128_f8f6f4 v[158:161], v[10:15], v[182:187], v[158:161], v16, v188 op_sel_hi:[0,0,0] cbsz:2 blgp:2
	v_mfma_scale_f32_16x16x128_f8f6f4 v[154:157], v[2:7], v[190:195], v[154:157], v8, v196 op_sel_hi:[0,0,0] cbsz:2 blgp:2
	v_mfma_scale_f32_16x16x128_f8f6f4 v[150:153], v[10:15], v[190:195], v[150:153], v16, v196 op_sel_hi:[0,0,0] cbsz:2 blgp:2
	s_setprio 0
	s_setprio 1
	v_mfma_scale_f32_16x16x128_f8f6f4 v[146:149], v[18:23], v[34:39], v[146:149], v24, v40 op_sel_hi:[0,0,0] cbsz:2 blgp:2
	v_mfma_scale_f32_16x16x128_f8f6f4 v[142:145], v[26:31], v[34:39], v[142:145], v32, v40 op_sel_hi:[0,0,0] cbsz:2 blgp:2
	v_mfma_scale_f32_16x16x128_f8f6f4 v[138:141], v[18:23], v[42:47], v[138:141], v24, v48 op_sel_hi:[0,0,0] cbsz:2 blgp:2
	v_mfma_scale_f32_16x16x128_f8f6f4 v[134:137], v[26:31], v[42:47], v[134:137], v32, v48 op_sel_hi:[0,0,0] cbsz:2 blgp:2
	v_mfma_scale_f32_16x16x128_f8f6f4 v[130:133], v[18:23], v[182:187], v[130:133], v24, v188 op_sel_hi:[0,0,0] cbsz:2 blgp:2
	v_mfma_scale_f32_16x16x128_f8f6f4 v[126:129], v[26:31], v[182:187], v[126:129], v32, v188 op_sel_hi:[0,0,0] cbsz:2 blgp:2
	v_mfma_scale_f32_16x16x128_f8f6f4 v[122:125], v[18:23], v[190:195], v[122:125], v24, v196 op_sel_hi:[0,0,0] cbsz:2 blgp:2
	v_mfma_scale_f32_16x16x128_f8f6f4 v[118:121], v[26:31], v[190:195], v[118:121], v32, v196 op_sel_hi:[0,0,0] cbsz:2 blgp:2
	s_setprio 0
	s_barrier
	ds_read_b128 v[34:37], v227 offset:16384
	ds_read_b128 v[38:41], v227 offset:17408
	ds_read_b128 v[42:45], v227 offset:18432
	ds_read_b128 v[46:49], v227 offset:19456
	ds_read_b128 v[182:185], v227 offset:20480
	ds_read_b128 v[186:189], v227 offset:21504
	ds_read_b128 v[190:193], v227 offset:22528
	ds_read_b128 v[194:197], v227 offset:23552
	s_mov_b32 m0, s47
	s_nop 0
	global_load_lds_dwordx4 v219, s[10:11]
	s_nop 0
	s_mov_b32 m0, s53
	s_nop 0
	global_load_lds_dwordx4 v221, s[10:11]
	s_waitcnt vmcnt(12)
	s_waitcnt lgkmcnt(0)
	s_barrier
	s_setprio 1
	v_mfma_scale_f32_16x16x128_f8f6f4 v[114:117], v[2:7], v[34:39], v[114:117], v8, v40 op_sel_hi:[0,0,0] cbsz:2 blgp:2
	v_mfma_scale_f32_16x16x128_f8f6f4 v[110:113], v[10:15], v[34:39], v[110:113], v16, v40 op_sel_hi:[0,0,0] cbsz:2 blgp:2
	s_mov_b32 m0, s48
	s_nop 0
	global_load_lds_dwordx4 v214, s[26:27]
	v_mfma_scale_f32_16x16x128_f8f6f4 v[106:109], v[2:7], v[42:47], v[106:109], v8, v48 op_sel_hi:[0,0,0] cbsz:2 blgp:2
	v_mfma_scale_f32_16x16x128_f8f6f4 v[102:105], v[10:15], v[42:47], v[102:105], v16, v48 op_sel_hi:[0,0,0] cbsz:2 blgp:2
	s_mov_b32 m0, s49
	s_nop 0
	global_load_lds_dwordx4 v215, s[26:27]
	s_add_u32 s26, s6, 0x40100
	s_addc_u32 s27, s7, 0
	v_mfma_scale_f32_16x16x128_f8f6f4 v[98:101], v[2:7], v[182:187], v[98:101], v8, v188 op_sel_hi:[0,0,0] cbsz:2 blgp:2
	v_mfma_scale_f32_16x16x128_f8f6f4 v[94:97], v[10:15], v[182:187], v[94:97], v16, v188 op_sel_hi:[0,0,0] cbsz:2 blgp:2
	v_mfma_scale_f32_16x16x128_f8f6f4 v[90:93], v[2:7], v[190:195], v[90:93], v8, v196 op_sel_hi:[0,0,0] cbsz:2 blgp:2
	v_mfma_scale_f32_16x16x128_f8f6f4 v[86:89], v[10:15], v[190:195], v[86:89], v16, v196 op_sel_hi:[0,0,0] cbsz:2 blgp:2
	s_setprio 0
	s_setprio 1
	v_mfma_scale_f32_16x16x128_f8f6f4 v[82:85], v[18:23], v[34:39], v[82:85], v24, v40 op_sel_hi:[0,0,0] cbsz:2 blgp:2
	v_mfma_scale_f32_16x16x128_f8f6f4 v[78:81], v[26:31], v[34:39], v[78:81], v32, v40 op_sel_hi:[0,0,0] cbsz:2 blgp:2
	s_mov_b32 m0, s51
	s_nop 0
	global_load_lds_dwordx4 v214, s[26:27]
	v_mfma_scale_f32_16x16x128_f8f6f4 v[74:77], v[18:23], v[42:47], v[74:77], v24, v48 op_sel_hi:[0,0,0] cbsz:2 blgp:2
	v_mfma_scale_f32_16x16x128_f8f6f4 v[70:73], v[26:31], v[42:47], v[70:73], v32, v48 op_sel_hi:[0,0,0] cbsz:2 blgp:2
	s_mov_b32 m0, s52
	s_nop 0
	global_load_lds_dwordx4 v215, s[26:27]
	v_mfma_scale_f32_16x16x128_f8f6f4 v[66:69], v[18:23], v[182:187], v[66:69], v24, v188 op_sel_hi:[0,0,0] cbsz:2 blgp:2
	v_mfma_scale_f32_16x16x128_f8f6f4 v[62:65], v[26:31], v[182:187], v[62:65], v32, v188 op_sel_hi:[0,0,0] cbsz:2 blgp:2
	v_mfma_scale_f32_16x16x128_f8f6f4 v[58:61], v[18:23], v[190:195], v[58:61], v24, v196 op_sel_hi:[0,0,0] cbsz:2 blgp:2
	v_mfma_scale_f32_16x16x128_f8f6f4 v[54:57], v[26:31], v[190:195], v[54:57], v32, v196 op_sel_hi:[0,0,0] cbsz:2 blgp:2
	s_setprio 0
	s_barrier
	ds_read_b128 v[2:5], v53
	ds_read_b128 v[6:9], v53 offset:1024
	ds_read_b128 v[10:13], v53 offset:2048
	ds_read_b128 v[14:17], v53 offset:3072
	ds_read_b128 v[18:21], v229
	ds_read_b128 v[22:25], v229 offset:1024
	ds_read_b128 v[26:29], v229 offset:2048
	ds_read_b128 v[30:33], v229 offset:3072
	ds_read_b128 v[34:37], v227 offset:32768
	ds_read_b128 v[38:41], v227 offset:33792
	ds_read_b128 v[42:45], v227 offset:34816
	ds_read_b128 v[46:49], v227 offset:35840
	ds_read_b128 v[182:185], v227 offset:36864
	ds_read_b128 v[186:189], v227 offset:37888
	ds_read_b128 v[190:193], v227 offset:38912
	ds_read_b128 v[194:197], v227 offset:39936
	s_mov_b32 m0, s54
	s_nop 0
	global_load_lds_dwordx4 v220, s[10:11]
	s_nop 0
	s_mov_b32 m0, s55
	s_nop 0
	global_load_lds_dwordx4 v222, s[10:11]
	s_waitcnt vmcnt(8)
	s_waitcnt lgkmcnt(0)
	s_barrier
	s_setprio 1
	v_mfma_scale_f32_16x16x128_f8f6f4 v[178:181], v[2:7], v[34:39], v[178:181], v8, v40 op_sel_hi:[0,0,0] cbsz:2 blgp:2
	v_mfma_scale_f32_16x16x128_f8f6f4 v[174:177], v[10:15], v[34:39], v[174:177], v16, v40 op_sel_hi:[0,0,0] cbsz:2 blgp:2
	v_mfma_scale_f32_16x16x128_f8f6f4 v[170:173], v[2:7], v[42:47], v[170:173], v8, v48 op_sel_hi:[0,0,0] cbsz:2 blgp:2
	v_mfma_scale_f32_16x16x128_f8f6f4 v[166:169], v[10:15], v[42:47], v[166:169], v16, v48 op_sel_hi:[0,0,0] cbsz:2 blgp:2
	v_mfma_scale_f32_16x16x128_f8f6f4 v[162:165], v[2:7], v[182:187], v[162:165], v8, v188 op_sel_hi:[0,0,0] cbsz:2 blgp:2
	v_mfma_scale_f32_16x16x128_f8f6f4 v[158:161], v[10:15], v[182:187], v[158:161], v16, v188 op_sel_hi:[0,0,0] cbsz:2 blgp:2
	v_mfma_scale_f32_16x16x128_f8f6f4 v[154:157], v[2:7], v[190:195], v[154:157], v8, v196 op_sel_hi:[0,0,0] cbsz:2 blgp:2
	v_mfma_scale_f32_16x16x128_f8f6f4 v[150:153], v[10:15], v[190:195], v[150:153], v16, v196 op_sel_hi:[0,0,0] cbsz:2 blgp:2
	s_setprio 0
	s_setprio 1
	v_mfma_scale_f32_16x16x128_f8f6f4 v[146:149], v[18:23], v[34:39], v[146:149], v24, v40 op_sel_hi:[0,0,0] cbsz:2 blgp:2
	v_mfma_scale_f32_16x16x128_f8f6f4 v[142:145], v[26:31], v[34:39], v[142:145], v32, v40 op_sel_hi:[0,0,0] cbsz:2 blgp:2
	v_mfma_scale_f32_16x16x128_f8f6f4 v[138:141], v[18:23], v[42:47], v[138:141], v24, v48 op_sel_hi:[0,0,0] cbsz:2 blgp:2
	v_mfma_scale_f32_16x16x128_f8f6f4 v[134:137], v[26:31], v[42:47], v[134:137], v32, v48 op_sel_hi:[0,0,0] cbsz:2 blgp:2
	v_mfma_scale_f32_16x16x128_f8f6f4 v[130:133], v[18:23], v[182:187], v[130:133], v24, v188 op_sel_hi:[0,0,0] cbsz:2 blgp:2
	v_mfma_scale_f32_16x16x128_f8f6f4 v[126:129], v[26:31], v[182:187], v[126:129], v32, v188 op_sel_hi:[0,0,0] cbsz:2 blgp:2
	v_mfma_scale_f32_16x16x128_f8f6f4 v[122:125], v[18:23], v[190:195], v[122:125], v24, v196 op_sel_hi:[0,0,0] cbsz:2 blgp:2
	v_mfma_scale_f32_16x16x128_f8f6f4 v[118:121], v[26:31], v[190:195], v[118:121], v32, v196 op_sel_hi:[0,0,0] cbsz:2 blgp:2
	s_setprio 0
	s_barrier
	ds_read_b128 v[34:37], v227 offset:49152
	ds_read_b128 v[38:41], v227 offset:50176
	ds_read_b128 v[42:45], v227 offset:51200
	ds_read_b128 v[46:49], v227 offset:52224
	ds_read_b128 v[182:185], v227 offset:53248
	ds_read_b128 v[186:189], v227 offset:54272
	ds_read_b128 v[190:193], v227 offset:55296
	ds_read_b128 v[194:197], v227 offset:56320
	s_mov_b32 m0, s58
	s_nop 0
	global_load_lds_dwordx4 v219, s[12:13]
	s_nop 0
	s_mov_b32 m0, s59
	s_nop 0
	global_load_lds_dwordx4 v221, s[12:13]
	s_waitcnt vmcnt(4)
	s_waitcnt lgkmcnt(0)
	s_barrier
	s_setprio 1
	s_add_u32 s26, s6, 0x180
	s_addc_u32 s27, s7, 0
	v_mfma_scale_f32_16x16x128_f8f6f4 v[114:117], v[2:7], v[34:39], v[114:117], v8, v40 op_sel_hi:[0,0,0] cbsz:2 blgp:2
	v_mfma_scale_f32_16x16x128_f8f6f4 v[110:113], v[10:15], v[34:39], v[110:113], v16, v40 op_sel_hi:[0,0,0] cbsz:2 blgp:2
	s_mov_b32 m0, s56
	s_nop 0
	global_load_lds_dwordx4 v214, s[26:27]
	v_mfma_scale_f32_16x16x128_f8f6f4 v[106:109], v[2:7], v[42:47], v[106:109], v8, v48 op_sel_hi:[0,0,0] cbsz:2 blgp:2
	v_mfma_scale_f32_16x16x128_f8f6f4 v[102:105], v[10:15], v[42:47], v[102:105], v16, v48 op_sel_hi:[0,0,0] cbsz:2 blgp:2
	s_mov_b32 m0, s57
	s_nop 0
	global_load_lds_dwordx4 v215, s[26:27]
	s_add_u32 s26, s6, 0x40180
	s_addc_u32 s27, s7, 0
	v_mfma_scale_f32_16x16x128_f8f6f4 v[98:101], v[2:7], v[182:187], v[98:101], v8, v188 op_sel_hi:[0,0,0] cbsz:2 blgp:2
	v_mfma_scale_f32_16x16x128_f8f6f4 v[94:97], v[10:15], v[182:187], v[94:97], v16, v188 op_sel_hi:[0,0,0] cbsz:2 blgp:2
	v_mfma_scale_f32_16x16x128_f8f6f4 v[90:93], v[2:7], v[190:195], v[90:93], v8, v196 op_sel_hi:[0,0,0] cbsz:2 blgp:2
	v_mfma_scale_f32_16x16x128_f8f6f4 v[86:89], v[10:15], v[190:195], v[86:89], v16, v196 op_sel_hi:[0,0,0] cbsz:2 blgp:2
	s_setprio 0
	s_setprio 1
	v_mfma_scale_f32_16x16x128_f8f6f4 v[82:85], v[18:23], v[34:39], v[82:85], v24, v40 op_sel_hi:[0,0,0] cbsz:2 blgp:2
	v_mfma_scale_f32_16x16x128_f8f6f4 v[78:81], v[26:31], v[34:39], v[78:81], v32, v40 op_sel_hi:[0,0,0] cbsz:2 blgp:2
	s_mov_b32 m0, s60
	s_nop 0
	global_load_lds_dwordx4 v214, s[26:27]
	v_mfma_scale_f32_16x16x128_f8f6f4 v[74:77], v[18:23], v[42:47], v[74:77], v24, v48 op_sel_hi:[0,0,0] cbsz:2 blgp:2
	v_mfma_scale_f32_16x16x128_f8f6f4 v[70:73], v[26:31], v[42:47], v[70:73], v32, v48 op_sel_hi:[0,0,0] cbsz:2 blgp:2
	s_mov_b32 m0, s61
	s_nop 0
	global_load_lds_dwordx4 v215, s[26:27]
	v_mfma_scale_f32_16x16x128_f8f6f4 v[66:69], v[18:23], v[182:187], v[66:69], v24, v188 op_sel_hi:[0,0,0] cbsz:2 blgp:2
	v_mfma_scale_f32_16x16x128_f8f6f4 v[62:65], v[26:31], v[182:187], v[62:65], v32, v188 op_sel_hi:[0,0,0] cbsz:2 blgp:2
	v_mfma_scale_f32_16x16x128_f8f6f4 v[58:61], v[18:23], v[190:195], v[58:61], v24, v196 op_sel_hi:[0,0,0] cbsz:2 blgp:2
	v_mfma_scale_f32_16x16x128_f8f6f4 v[54:57], v[26:31], v[190:195], v[54:57], v32, v196 op_sel_hi:[0,0,0] cbsz:2 blgp:2
	s_setprio 0
	s_barrier
	s_mov_b32 s28, 2
	s_branch .LBB0_1998

.LBB0_1999:
	s_add_i32 s38, s36, 0xe08c0100
	s_and_b64 s[36:37], s[34:35], exec
	s_cselect_b32 s77, s38, 0
	s_add_u32 s36, s41, s40
	s_addc_u32 s37, s76, 0
	s_waitcnt vmcnt(8)
	s_and_b64 s[34:35], s[34:35], exec
	s_waitcnt lgkmcnt(0)
	s_cselect_b32 s34, s36, s23
	s_cselect_b32 s35, s37, s2
	s_add_u32 s36, s34, 0x80
	s_addc_u32 s37, s35, 0
	s_barrier
	s_setprio 1
	v_mfma_scale_f32_16x16x128_f8f6f4 v[178:181], v[18:23], v[190:195], v[178:181], v24, v196 op_sel_hi:[0,0,0] cbsz:2 blgp:2
	v_mfma_scale_f32_16x16x128_f8f6f4 v[174:177], v[26:31], v[190:195], v[174:177], v32, v196 op_sel_hi:[0,0,0] cbsz:2 blgp:2
	v_mfma_scale_f32_16x16x128_f8f6f4 v[170:173], v[18:23], v[182:187], v[170:173], v24, v188 op_sel_hi:[0,0,0] cbsz:2 blgp:2
	v_mfma_scale_f32_16x16x128_f8f6f4 v[166:169], v[26:31], v[182:187], v[166:169], v32, v188 op_sel_hi:[0,0,0] cbsz:2 blgp:2
	v_mfma_scale_f32_16x16x128_f8f6f4 v[162:165], v[18:23], v[42:47], v[162:165], v24, v48 op_sel_hi:[0,0,0] cbsz:2 blgp:2
	v_mfma_scale_f32_16x16x128_f8f6f4 v[158:161], v[26:31], v[42:47], v[158:161], v32, v48 op_sel_hi:[0,0,0] cbsz:2 blgp:2
	v_mfma_scale_f32_16x16x128_f8f6f4 v[154:157], v[18:23], v[34:39], v[154:157], v24, v40 op_sel_hi:[0,0,0] cbsz:2 blgp:2
	v_mfma_scale_f32_16x16x128_f8f6f4 v[150:153], v[26:31], v[34:39], v[150:153], v32, v40 op_sel_hi:[0,0,0] cbsz:2 blgp:2
	s_setprio 0
	s_setprio 1
	v_mfma_scale_f32_16x16x128_f8f6f4 v[146:149], v[2:7], v[190:195], v[146:149], v8, v196 op_sel_hi:[0,0,0] cbsz:2 blgp:2
	v_mfma_scale_f32_16x16x128_f8f6f4 v[142:145], v[10:15], v[190:195], v[142:145], v16, v196 op_sel_hi:[0,0,0] cbsz:2 blgp:2
	v_mfma_scale_f32_16x16x128_f8f6f4 v[138:141], v[2:7], v[182:187], v[138:141], v8, v188 op_sel_hi:[0,0,0] cbsz:2 blgp:2
	v_mfma_scale_f32_16x16x128_f8f6f4 v[134:137], v[10:15], v[182:187], v[134:137], v16, v188 op_sel_hi:[0,0,0] cbsz:2 blgp:2
	v_mfma_scale_f32_16x16x128_f8f6f4 v[130:133], v[2:7], v[42:47], v[130:133], v8, v48 op_sel_hi:[0,0,0] cbsz:2 blgp:2
	v_mfma_scale_f32_16x16x128_f8f6f4 v[126:129], v[10:15], v[42:47], v[126:129], v16, v48 op_sel_hi:[0,0,0] cbsz:2 blgp:2
	v_mfma_scale_f32_16x16x128_f8f6f4 v[122:125], v[2:7], v[34:39], v[122:125], v8, v40 op_sel_hi:[0,0,0] cbsz:2 blgp:2
	v_mfma_scale_f32_16x16x128_f8f6f4 v[118:121], v[10:15], v[34:39], v[118:121], v16, v40 op_sel_hi:[0,0,0] cbsz:2 blgp:2
	s_setprio 0
	s_barrier
	ds_read_b128 v[34:37], v227 offset:16384
	ds_read_b128 v[38:41], v227 offset:17408
	ds_read_b128 v[42:45], v227 offset:18432
	ds_read_b128 v[46:49], v227 offset:19456
	ds_read_b128 v[182:185], v227 offset:20480
	ds_read_b128 v[186:189], v227 offset:21504
	ds_read_b128 v[190:193], v227 offset:22528
	ds_read_b128 v[194:197], v227 offset:23552
	s_add_u32 s38, s4, s77
	s_addc_u32 s39, s5, 0
	s_mov_b32 m0, s47
	s_nop 0
	global_load_lds_dwordx4 v219, s[38:39]
	s_nop 0
	s_mov_b32 m0, s53
	s_nop 0
	global_load_lds_dwordx4 v221, s[38:39]
	s_waitcnt vmcnt(4)
	s_waitcnt lgkmcnt(0)
	s_barrier
	s_setprio 1
	v_mfma_scale_f32_16x16x128_f8f6f4 v[114:117], v[18:23], v[34:39], v[114:117], v24, v40 op_sel_hi:[0,0,0] cbsz:2 blgp:2
	v_mfma_scale_f32_16x16x128_f8f6f4 v[110:113], v[26:31], v[34:39], v[110:113], v32, v40 op_sel_hi:[0,0,0] cbsz:2 blgp:2
	s_mov_b32 m0, s48
	s_nop 0
	global_load_lds_dwordx4 v214, s[34:35]
	v_mfma_scale_f32_16x16x128_f8f6f4 v[106:109], v[18:23], v[42:47], v[106:109], v24, v48 op_sel_hi:[0,0,0] cbsz:2 blgp:2
	v_mfma_scale_f32_16x16x128_f8f6f4 v[102:105], v[26:31], v[42:47], v[102:105], v32, v48 op_sel_hi:[0,0,0] cbsz:2 blgp:2
	s_add_u32 s100, s34, 0x40000
	s_addc_u32 s101, s35, 0
	s_mov_b32 m0, s49
	s_nop 0
	global_load_lds_dwordx4 v215, s[34:35]
	v_mfma_scale_f32_16x16x128_f8f6f4 v[98:101], v[18:23], v[182:187], v[98:101], v24, v188 op_sel_hi:[0,0,0] cbsz:2 blgp:2
	v_mfma_scale_f32_16x16x128_f8f6f4 v[94:97], v[26:31], v[182:187], v[94:97], v32, v188 op_sel_hi:[0,0,0] cbsz:2 blgp:2
	v_mfma_scale_f32_16x16x128_f8f6f4 v[90:93], v[18:23], v[190:195], v[90:93], v24, v196 op_sel_hi:[0,0,0] cbsz:2 blgp:2
	v_mfma_scale_f32_16x16x128_f8f6f4 v[86:89], v[26:31], v[190:195], v[86:89], v32, v196 op_sel_hi:[0,0,0] cbsz:2 blgp:2
	s_setprio 0
	s_setprio 1
	v_mfma_scale_f32_16x16x128_f8f6f4 v[82:85], v[2:7], v[34:39], v[82:85], v8, v40 op_sel_hi:[0,0,0] cbsz:2 blgp:2
	v_mfma_scale_f32_16x16x128_f8f6f4 v[78:81], v[10:15], v[34:39], v[78:81], v16, v40 op_sel_hi:[0,0,0] cbsz:2 blgp:2
	s_mov_b32 m0, s51
	s_nop 0
	global_load_lds_dwordx4 v214, s[100:101]
	v_mfma_scale_f32_16x16x128_f8f6f4 v[74:77], v[2:7], v[42:47], v[74:77], v8, v48 op_sel_hi:[0,0,0] cbsz:2 blgp:2
	v_mfma_scale_f32_16x16x128_f8f6f4 v[70:73], v[10:15], v[42:47], v[70:73], v16, v48 op_sel_hi:[0,0,0] cbsz:2 blgp:2
	s_mov_b32 m0, s52
	s_nop 0
	global_load_lds_dwordx4 v215, s[100:101]
	v_mfma_scale_f32_16x16x128_f8f6f4 v[66:69], v[2:7], v[182:187], v[66:69], v8, v188 op_sel_hi:[0,0,0] cbsz:2 blgp:2
	v_mfma_scale_f32_16x16x128_f8f6f4 v[62:65], v[10:15], v[182:187], v[62:65], v16, v188 op_sel_hi:[0,0,0] cbsz:2 blgp:2
	v_mfma_scale_f32_16x16x128_f8f6f4 v[58:61], v[2:7], v[190:195], v[58:61], v8, v196 op_sel_hi:[0,0,0] cbsz:2 blgp:2
	v_mfma_scale_f32_16x16x128_f8f6f4 v[54:57], v[10:15], v[190:195], v[54:57], v16, v196 op_sel_hi:[0,0,0] cbsz:2 blgp:2
	s_setprio 0
	s_barrier
	ds_read_b128 v[2:5], v53
	ds_read_b128 v[6:9], v53 offset:1024
	ds_read_b128 v[10:13], v53 offset:2048
	ds_read_b128 v[14:17], v53 offset:3072
	ds_read_b128 v[18:21], v229
	ds_read_b128 v[22:25], v229 offset:1024
	ds_read_b128 v[26:29], v229 offset:2048
	ds_read_b128 v[30:33], v229 offset:3072
	ds_read_b128 v[34:37], v227 offset:32768
	ds_read_b128 v[38:41], v227 offset:33792
	ds_read_b128 v[42:45], v227 offset:34816
	ds_read_b128 v[46:49], v227 offset:35840
	ds_read_b128 v[182:185], v227 offset:36864
	ds_read_b128 v[186:189], v227 offset:37888
	ds_read_b128 v[190:193], v227 offset:38912
	ds_read_b128 v[194:197], v227 offset:39936
	s_mov_b32 m0, s54
	s_nop 0
	global_load_lds_dwordx4 v220, s[38:39]
	s_nop 0
	s_mov_b32 m0, s55
	s_nop 0
	global_load_lds_dwordx4 v222, s[38:39]
	s_waitcnt vmcnt(8)
	s_waitcnt lgkmcnt(0)
	s_barrier
	s_setprio 1
	v_mfma_scale_f32_16x16x128_f8f6f4 v[178:181], v[2:7], v[34:39], v[178:181], v8, v40 op_sel_hi:[0,0,0] cbsz:2 blgp:2
	v_mfma_scale_f32_16x16x128_f8f6f4 v[174:177], v[10:15], v[34:39], v[174:177], v16, v40 op_sel_hi:[0,0,0] cbsz:2 blgp:2
	v_mfma_scale_f32_16x16x128_f8f6f4 v[170:173], v[2:7], v[42:47], v[170:173], v8, v48 op_sel_hi:[0,0,0] cbsz:2 blgp:2
	v_mfma_scale_f32_16x16x128_f8f6f4 v[166:169], v[10:15], v[42:47], v[166:169], v16, v48 op_sel_hi:[0,0,0] cbsz:2 blgp:2
	v_mfma_scale_f32_16x16x128_f8f6f4 v[162:165], v[2:7], v[182:187], v[162:165], v8, v188 op_sel_hi:[0,0,0] cbsz:2 blgp:2
	v_mfma_scale_f32_16x16x128_f8f6f4 v[158:161], v[10:15], v[182:187], v[158:161], v16, v188 op_sel_hi:[0,0,0] cbsz:2 blgp:2
	v_mfma_scale_f32_16x16x128_f8f6f4 v[154:157], v[2:7], v[190:195], v[154:157], v8, v196 op_sel_hi:[0,0,0] cbsz:2 blgp:2
	v_mfma_scale_f32_16x16x128_f8f6f4 v[150:153], v[10:15], v[190:195], v[150:153], v16, v196 op_sel_hi:[0,0,0] cbsz:2 blgp:2
	s_setprio 0
	s_setprio 1
	v_mfma_scale_f32_16x16x128_f8f6f4 v[146:149], v[18:23], v[34:39], v[146:149], v24, v40 op_sel_hi:[0,0,0] cbsz:2 blgp:2
	v_mfma_scale_f32_16x16x128_f8f6f4 v[142:145], v[26:31], v[34:39], v[142:145], v32, v40 op_sel_hi:[0,0,0] cbsz:2 blgp:2
	v_mfma_scale_f32_16x16x128_f8f6f4 v[138:141], v[18:23], v[42:47], v[138:141], v24, v48 op_sel_hi:[0,0,0] cbsz:2 blgp:2
	v_mfma_scale_f32_16x16x128_f8f6f4 v[134:137], v[26:31], v[42:47], v[134:137], v32, v48 op_sel_hi:[0,0,0] cbsz:2 blgp:2
	v_mfma_scale_f32_16x16x128_f8f6f4 v[130:133], v[18:23], v[182:187], v[130:133], v24, v188 op_sel_hi:[0,0,0] cbsz:2 blgp:2
	v_mfma_scale_f32_16x16x128_f8f6f4 v[126:129], v[26:31], v[182:187], v[126:129], v32, v188 op_sel_hi:[0,0,0] cbsz:2 blgp:2
	v_mfma_scale_f32_16x16x128_f8f6f4 v[122:125], v[18:23], v[190:195], v[122:125], v24, v196 op_sel_hi:[0,0,0] cbsz:2 blgp:2
	v_mfma_scale_f32_16x16x128_f8f6f4 v[118:121], v[26:31], v[190:195], v[118:121], v32, v196 op_sel_hi:[0,0,0] cbsz:2 blgp:2
	s_setprio 0
	s_barrier
	ds_read_b128 v[34:37], v227 offset:49152
	ds_read_b128 v[38:41], v227 offset:50176
	ds_read_b128 v[42:45], v227 offset:51200
	ds_read_b128 v[46:49], v227 offset:52224
	ds_read_b128 v[182:185], v227 offset:53248
	ds_read_b128 v[186:189], v227 offset:54272
	ds_read_b128 v[190:193], v227 offset:55296
	ds_read_b128 v[194:197], v227 offset:56320
	s_add_u32 s100, s38, 0x80
	s_addc_u32 s101, s39, 0
	s_mov_b32 m0, s58
	s_nop 0
	global_load_lds_dwordx4 v219, s[100:101]
	s_nop 0
	s_mov_b32 m0, s59
	s_nop 0
	global_load_lds_dwordx4 v221, s[100:101]
	s_waitcnt vmcnt(4)
	s_waitcnt lgkmcnt(0)
	s_barrier
	s_setprio 1
	v_mfma_scale_f32_16x16x128_f8f6f4 v[114:117], v[2:7], v[34:39], v[114:117], v8, v40 op_sel_hi:[0,0,0] cbsz:2 blgp:2
	v_mfma_scale_f32_16x16x128_f8f6f4 v[110:113], v[10:15], v[34:39], v[110:113], v16, v40 op_sel_hi:[0,0,0] cbsz:2 blgp:2
	s_mov_b32 m0, s56
	s_nop 0
	global_load_lds_dwordx4 v214, s[36:37]
	v_mfma_scale_f32_16x16x128_f8f6f4 v[106:109], v[2:7], v[42:47], v[106:109], v8, v48 op_sel_hi:[0,0,0] cbsz:2 blgp:2
	v_mfma_scale_f32_16x16x128_f8f6f4 v[102:105], v[10:15], v[42:47], v[102:105], v16, v48 op_sel_hi:[0,0,0] cbsz:2 blgp:2
	s_mov_b32 m0, s57
	s_nop 0
	global_load_lds_dwordx4 v215, s[36:37]
	s_add_u32 s34, s34, 0x40080
	s_addc_u32 s35, s35, 0
	v_mfma_scale_f32_16x16x128_f8f6f4 v[98:101], v[2:7], v[182:187], v[98:101], v8, v188 op_sel_hi:[0,0,0] cbsz:2 blgp:2
	v_mfma_scale_f32_16x16x128_f8f6f4 v[94:97], v[10:15], v[182:187], v[94:97], v16, v188 op_sel_hi:[0,0,0] cbsz:2 blgp:2
	v_mfma_scale_f32_16x16x128_f8f6f4 v[90:93], v[2:7], v[190:195], v[90:93], v8, v196 op_sel_hi:[0,0,0] cbsz:2 blgp:2
	v_mfma_scale_f32_16x16x128_f8f6f4 v[86:89], v[10:15], v[190:195], v[86:89], v16, v196 op_sel_hi:[0,0,0] cbsz:2 blgp:2
	s_setprio 0
	s_setprio 1
	v_mfma_scale_f32_16x16x128_f8f6f4 v[82:85], v[18:23], v[34:39], v[82:85], v24, v40 op_sel_hi:[0,0,0] cbsz:2 blgp:2
	v_mfma_scale_f32_16x16x128_f8f6f4 v[78:81], v[26:31], v[34:39], v[78:81], v32, v40 op_sel_hi:[0,0,0] cbsz:2 blgp:2
	s_mov_b32 m0, s60
	s_nop 0
	global_load_lds_dwordx4 v214, s[34:35]
	v_mfma_scale_f32_16x16x128_f8f6f4 v[74:77], v[18:23], v[42:47], v[74:77], v24, v48 op_sel_hi:[0,0,0] cbsz:2 blgp:2
	v_mfma_scale_f32_16x16x128_f8f6f4 v[70:73], v[26:31], v[42:47], v[70:73], v32, v48 op_sel_hi:[0,0,0] cbsz:2 blgp:2
	s_mov_b32 m0, s61
	s_nop 0
	global_load_lds_dwordx4 v215, s[34:35]
	v_mfma_scale_f32_16x16x128_f8f6f4 v[66:69], v[18:23], v[182:187], v[66:69], v24, v188 op_sel_hi:[0,0,0] cbsz:2 blgp:2
	v_mfma_scale_f32_16x16x128_f8f6f4 v[62:65], v[26:31], v[182:187], v[62:65], v32, v188 op_sel_hi:[0,0,0] cbsz:2 blgp:2
	v_mfma_scale_f32_16x16x128_f8f6f4 v[58:61], v[18:23], v[190:195], v[58:61], v24, v196 op_sel_hi:[0,0,0] cbsz:2 blgp:2
	v_mfma_scale_f32_16x16x128_f8f6f4 v[54:57], v[26:31], v[190:195], v[54:57], v32, v196 op_sel_hi:[0,0,0] cbsz:2 blgp:2
	s_setprio 0
	s_barrier
	s_add_i32 s33, s33, 2
	s_add_u32 s41, s41, 0x100
	s_addc_u32 s76, s76, 0
	s_add_u32 s30, s30, 0x100
	s_addc_u32 s31, s31, 0
	s_add_u32 s28, s28, 0x100
	s_addc_u32 s29, s29, 0
	s_cmp_gt_u32 s33, 13
	s_cbranch_scc1 .LBB0_2002
.LBB0_2000:
	ds_read_b128 v[18:21], v51
	ds_read_b128 v[22:25], v51 offset:1024
	ds_read_b128 v[26:29], v51 offset:2048
	ds_read_b128 v[30:33], v51 offset:3072
	ds_read_b128 v[2:5], v52
	ds_read_b128 v[6:9], v52 offset:1024
	ds_read_b128 v[10:13], v52 offset:2048
	ds_read_b128 v[14:17], v52 offset:3072
	s_add_u32 s36, s40, s28
	s_cmp_lg_u32 s36, 0x1f740700
	s_cselect_b64 s[34:35], -1, 0
	ds_read_b128 v[190:193], v227
	ds_read_b128 v[194:197], v227 offset:1024
	ds_read_b128 v[182:185], v227 offset:2048
	ds_read_b128 v[186:189], v227 offset:3072
	ds_read_b128 v[42:45], v227 offset:4096
	ds_read_b128 v[46:49], v227 offset:5120
	ds_read_b128 v[34:37], v227 offset:6144
	ds_read_b128 v[38:41], v227 offset:7168
	s_add_u32 s37, s30, s40
	s_addc_u32 s39, s31, 0
	s_add_u32 s38, s37, 0x80
	s_addc_u32 s39, s39, 0
	s_mov_b32 m0, s62
	s_nop 0
	global_load_lds_dwordx4 v220, s[38:39]
	s_nop 0
	s_mov_b32 m0, s63
	s_nop 0
	global_load_lds_dwordx4 v222, s[38:39]
	s_or_b64 s[38:39], s[18:19], s[34:35]
	s_and_b64 vcc, exec, s[38:39]
	s_cbranch_vccnz .LBB0_1999
	ds_read_u16 v198, v230
	ds_read_u16 v199, v230 offset:256
	ds_read_u16 v200, v231
	ds_read_u16 v201, v231 offset:256
	s_waitcnt lgkmcnt(3)
	v_lshl_or_b32 v219, v198, 11, v1
	s_waitcnt lgkmcnt(2)
	v_lshl_or_b32 v220, v199, 11, v1
	s_waitcnt lgkmcnt(1)
	v_lshl_or_b32 v221, v200, 11, v1
	s_waitcnt lgkmcnt(0)
	v_lshl_or_b32 v222, v201, 11, v1
	s_branch .LBB0_1999

; __global__ void __launch_bounds__(512, 2) mega(P p, int lo, int hi, int bar_idx) {
;     extern __shared__ __attribute__((aligned(16))) unsigned char lds_raw[];
	.amdhsa_kernel _Z4mega1Piii
		.amdhsa_group_segment_fixed_size 0
		.amdhsa_private_segment_fixed_size 0
		.amdhsa_kernarg_size 448
		.amdhsa_user_sgpr_count 2
		.amdhsa_user_sgpr_dispatch_ptr 0
		.amdhsa_user_sgpr_queue_ptr 0
		.amdhsa_user_sgpr_kernarg_segment_ptr 1
		.amdhsa_user_sgpr_dispatch_id 0
		.amdhsa_user_sgpr_kernarg_preload_length 0
		.amdhsa_user_sgpr_kernarg_preload_offset 0
		.amdhsa_user_sgpr_private_segment_size 0
		.amdhsa_uses_dynamic_stack 0
		.amdhsa_enable_private_segment 0
		.amdhsa_system_sgpr_workgroup_id_x 1
		.amdhsa_system_sgpr_workgroup_id_y 0
		.amdhsa_system_sgpr_workgroup_id_z 0
		.amdhsa_system_sgpr_workgroup_info 0
		.amdhsa_system_vgpr_workitem_id 0
		.amdhsa_next_free_vgpr 243
		.amdhsa_next_free_sgpr 102
		.amdhsa_accum_offset 244
		.amdhsa_reserve_vcc 1
		.amdhsa_float_round_mode_32 0
		.amdhsa_float_round_mode_16_64 0
		.amdhsa_float_denorm_mode_32 3
		.amdhsa_float_denorm_mode_16_64 3
		.amdhsa_dx10_clamp 1
		.amdhsa_ieee_mode 1
		.amdhsa_fp16_overflow 0
		.amdhsa_tg_split 0
		.amdhsa_exception_fp_ieee_invalid_op 0
		.amdhsa_exception_fp_denorm_src 0
		.amdhsa_exception_fp_ieee_div_zero 0
		.amdhsa_exception_fp_ieee_overflow 0
		.amdhsa_exception_fp_ieee_underflow 0
		.amdhsa_exception_fp_ieee_inexact 0
		.amdhsa_exception_int_div_zero 0
	.end_amdhsa_kernel

; __global__ void __launch_bounds__(512, 2) mega(P p, int lo, int hi, int bar_idx) {
amdhsa.kernels:
  - .agpr_count:     0
    .args:
      - .offset:         0
        .size:           176
        .value_kind:     by_value
      - .offset:         176
        .size:           4
        .value_kind:     by_value
      - .offset:         180
        .size:           4
        .value_kind:     by_value
      - .offset:         184
        .size:           4
        .value_kind:     by_value
      - .offset:         192
        .size:           4
        .value_kind:     hidden_block_count_x
      - .offset:         196
        .size:           4
        .value_kind:     hidden_block_count_y
      - .offset:         200
        .size:           4
        .value_kind:     hidden_block_count_z
      - .offset:         204
        .size:           2
        .value_kind:     hidden_group_size_x
      - .offset:         206
        .size:           2
        .value_kind:     hidden_group_size_y
      - .offset:         208
        .size:           2
        .value_kind:     hidden_group_size_z
      - .offset:         210
        .size:           2
        .value_kind:     hidden_remainder_x
      - .offset:         212
        .size:           2
        .value_kind:     hidden_remainder_y
      - .offset:         214
        .size:           2
        .value_kind:     hidden_remainder_z
      - .offset:         232
        .size:           8
        .value_kind:     hidden_global_offset_x
      - .offset:         240
        .size:           8
        .value_kind:     hidden_global_offset_y
      - .offset:         248
        .size:           8
        .value_kind:     hidden_global_offset_z
      - .offset:         256
        .size:           2
        .value_kind:     hidden_grid_dims
      - .offset:         312
        .size:           4
        .value_kind:     hidden_dynamic_lds_size
    .group_segment_fixed_size: 0
    .kernarg_segment_align: 8
    .kernarg_segment_size: 448
    .language:       OpenCL C
    .language_version:
      - 2
      - 0
    .max_flat_workgroup_size: 512
    .name:           _Z4mega1Piii
    .private_segment_fixed_size: 0
    .sgpr_count:     108
    .sgpr_spill_count: 174
    .symbol:         _Z4mega1Piii.kd
    .uniform_work_group_size: 1
    .uses_dynamic_stack: false
    .vgpr_count:     243
    .vgpr_spill_count: 0
    .wavefront_size: 64
